# layer-0 w_in phase re-split 136 conversion / 120 GEMM workgroups (multiple of 8 keeps the XCD-aware unit order; GEMM 9 rounds instead of 10) with the conversion loop's counted waits
# speedup vs baseline: 1.0100x; 1.0092x over previous
.LBB0_102:
	s_load_dwordx16 s[36:51], s[0:1], 0x40
	s_add_u32 s30, s16, 0x100000
	s_addc_u32 s31, s17, 0
	s_add_u32 s26, s16, 0x25313200
	s_addc_u32 s27, s17, 0
	s_waitcnt lgkmcnt(0)
	v_writelane_b32 v251, s36, 31
	s_cmpk_lt_i32 s96, 0x80
	s_cselect_b64 s[0:1], -1, 0
	v_writelane_b32 v251, s37, 32
	v_writelane_b32 v251, s38, 33
	v_writelane_b32 v251, s39, 34
	v_writelane_b32 v251, s40, 35
	v_writelane_b32 v251, s41, 36
	v_writelane_b32 v251, s42, 37
	v_writelane_b32 v251, s43, 38
	v_writelane_b32 v251, s44, 39
	v_writelane_b32 v251, s45, 40
	v_writelane_b32 v251, s46, 41
	v_writelane_b32 v251, s47, 42
	v_writelane_b32 v251, s48, 43
	v_writelane_b32 v251, s49, 44
	v_writelane_b32 v251, s50, 45
	v_writelane_b32 v251, s51, 46
	v_writelane_b32 v251, s0, 47
	v_mov_b32_e32 v3, 0
	v_mbcnt_lo_u32_b32 v1, -1, 0
	v_writelane_b32 v251, s1, 48
	s_lshr_b32 s0, s96, 31
	s_add_i32 s0, s96, s0
	s_lshl_b32 s1, s0, 6
	s_and_b32 s1, s1, 0xffffff80
	s_and_b32 s0, s0, -2
	s_sub_i32 s2, s96, s0
	v_writelane_b32 v251, s1, 49
	s_add_i32 s0, s1, 0x80
	v_writelane_b32 v251, s0, 50
	s_mov_b32 s0, s2
	s_ashr_i32 s3, s2, 31
	v_writelane_b32 v251, s0, 51
	v_mov_b32_e32 v228, 1
	v_mbcnt_hi_u32_b32 v229, -1, v1
	v_writelane_b32 v251, s1, 52
	s_lshl_b64 s[0:1], s[2:3], 20
	s_add_u32 s0, s26, s0
	s_addc_u32 s1, s27, s1
	s_add_u32 s2, s0, 0x4000
	s_addc_u32 s3, s1, 0
	v_writelane_b32 v251, s2, 53
	v_mov_b32_e32 v230, 0x358637bd
	v_mov_b32_e32 v231, 0x260
	v_writelane_b32 v251, s3, 54
	s_add_u32 s2, s0, 0x8000
	s_addc_u32 s3, s1, 0
	v_writelane_b32 v251, s2, 55
	v_mov_b32_e32 v232, 0x3727c5ac
	v_mov_b64_e32 v[202:203], 0xff
	v_writelane_b32 v251, s3, 56
	s_add_u32 s2, s16, 0x100080
	s_addc_u32 s3, s17, 0
	v_writelane_b32 v251, s2, 57
	v_mov_b32_e32 v233, 0x41b17218
	v_mov_b32_e32 v234, 0xf149f2ca
	v_writelane_b32 v251, s3, 58
	s_add_u32 s2, s0, 0xc000
	v_writelane_b32 v251, s0, 59
	s_addc_u32 s3, s1, 0
	v_mov_b32_e32 v235, 0x2200
	v_writelane_b32 v251, s1, 60
	v_writelane_b32 v251, s2, 61
	s_add_u32 s0, s16, 0x6102200
	s_addc_u32 s1, s17, 0
	v_writelane_b32 v251, s3, 62
	v_writelane_b32 v251, s0, 63
	v_mov_b32_e32 v84, v3
	v_mov_b32_e32 v85, v3
	v_writelane_b32 v252, s1, 0
	s_add_u32 s0, s16, 0x25514300
	v_writelane_b32 v252, s0, 1
	s_addc_u32 s0, s17, 0
	s_cmpk_lt_i32 s66, 0x100
	v_writelane_b32 v252, s0, 2
	s_cselect_b64 s[0:1], -1, 0
	v_writelane_b32 v252, s0, 3
	v_mov_b32_e32 v86, v3
	v_mov_b32_e32 v87, v3
	v_writelane_b32 v252, s1, 4
	s_ashr_i32 s0, s66, 31
	v_writelane_b32 v252, s0, 5
	s_lshr_b32 s0, s0, 29
	s_add_i32 s0, s66, s0
	s_ashr_i32 s2, s0, 3
	s_and_b32 s0, s0, -8
	s_sub_i32 s3, s66, s0
	s_lshl_b32 s4, s3, 5
	s_add_u32 s0, s16, 0x4200
	s_addc_u32 s1, s17, 0
	v_writelane_b32 v252, s0, 6
	v_mov_b32_e32 v236, 0x2000880
	v_mov_b32_e32 v237, 0x1000
	v_writelane_b32 v252, s1, 7
	s_add_u32 s0, s16, 0x4400
	s_addc_u32 s1, s17, 0
	v_writelane_b32 v252, s0, 8
	v_mov_b32_e32 v238, 0x1800
	s_movk_i32 s29, 0x80
	v_writelane_b32 v252, s1, 9
	s_add_u32 s0, s16, 0x4500
	s_addc_u32 s1, s17, 0
	v_writelane_b32 v252, s0, 10
	s_mov_b32 s90, 0
	s_mov_b32 s35, 0
	v_writelane_b32 v252, s1, 11
	s_add_u32 s0, s16, 0x4600
	s_addc_u32 s1, s17, 0
	v_writelane_b32 v252, s0, 12
	s_mov_b64 s[36:37], 0x80
	s_mov_b32 s46, 0x3e38aa3b
	v_writelane_b32 v252, s1, 13
	s_add_u32 s0, s16, 0x4700
	s_addc_u32 s1, s17, 0
	v_writelane_b32 v252, s0, 14
	s_mov_b32 s28, 0x3fd744fd
	s_nop 0
	v_writelane_b32 v252, s1, 15
	s_add_u32 s0, s16, 0x4800
	s_addc_u32 s1, s17, 0
	v_writelane_b32 v252, s0, 16
	s_nop 1
	v_writelane_b32 v252, s1, 17
	s_add_u32 s0, s16, 0x4900
	s_addc_u32 s1, s17, 0
	v_writelane_b32 v252, s0, 18
	s_nop 1
	v_writelane_b32 v252, s1, 19
	s_add_u32 s0, s16, 0x4a00
	s_addc_u32 s1, s17, 0
	v_writelane_b32 v252, s0, 20
	s_nop 1
	v_writelane_b32 v252, s1, 21
	s_add_u32 s0, s16, 0x4b00
	s_addc_u32 s1, s17, 0
	v_writelane_b32 v252, s0, 22
	s_nop 1
	v_writelane_b32 v252, s1, 23
	s_add_u32 s0, s16, 0x4c00
	s_addc_u32 s1, s17, 0
	v_writelane_b32 v252, s0, 24
	s_nop 1
	v_writelane_b32 v252, s1, 25
	s_add_u32 s0, s16, 0x4d00
	s_addc_u32 s1, s17, 0
	v_writelane_b32 v252, s0, 26
	s_nop 1
	v_writelane_b32 v252, s1, 27
	s_add_u32 s0, s16, 0x4e00
	s_addc_u32 s1, s17, 0
	v_writelane_b32 v252, s0, 28
	s_nop 1
	v_writelane_b32 v252, s1, 29
	s_add_u32 s0, s16, 0x4f00
	s_addc_u32 s1, s17, 0
	v_writelane_b32 v252, s0, 30
	s_nop 1
	v_writelane_b32 v252, s1, 31
	s_add_u32 s0, s16, 0x5000
	s_addc_u32 s1, s17, 0
	v_writelane_b32 v252, s0, 32
	s_nop 1
	v_writelane_b32 v252, s1, 33
	s_add_u32 s0, s16, 0x5100
	s_addc_u32 s1, s17, 0
	v_writelane_b32 v252, s0, 34
	s_nop 1
	v_writelane_b32 v252, s1, 35
	s_add_u32 s0, s16, 0x5200
	s_addc_u32 s1, s17, 0
	v_writelane_b32 v252, s0, 36
	s_nop 1
	v_writelane_b32 v252, s1, 37
	s_add_u32 s0, s16, 0x5300
	s_addc_u32 s1, s17, 0
	v_writelane_b32 v252, s0, 38
	s_cmp_eq_u32 s33, 15
	s_nop 0
	v_writelane_b32 v252, s1, 39
	s_cselect_b64 s[0:1], -1, 0
	v_writelane_b32 v252, s0, 40
	s_cmp_eq_u32 s33, 14
	s_nop 0
	v_writelane_b32 v252, s1, 41
	s_cselect_b64 s[0:1], -1, 0
	v_writelane_b32 v252, s0, 42
	s_cmp_eq_u32 s33, 13
	s_nop 0
	v_writelane_b32 v252, s1, 43
	s_cselect_b64 s[0:1], -1, 0
	v_writelane_b32 v252, s0, 44
	s_cmp_eq_u32 s33, 12
	s_nop 0
	v_writelane_b32 v252, s1, 45
	s_cselect_b64 s[0:1], -1, 0
	v_writelane_b32 v252, s0, 46
	s_cmp_eq_u32 s33, 11
	s_nop 0
	v_writelane_b32 v252, s1, 47
	s_cselect_b64 s[0:1], -1, 0
	v_writelane_b32 v252, s0, 48
	s_cmp_eq_u32 s33, 10
	s_nop 0
	v_writelane_b32 v252, s1, 49
	s_cselect_b64 s[0:1], -1, 0
	v_writelane_b32 v252, s0, 50
	s_cmp_eq_u32 s33, 9
	s_nop 0
	v_writelane_b32 v252, s1, 51
	s_cselect_b64 s[0:1], -1, 0
	v_writelane_b32 v252, s0, 52
	s_cmp_eq_u32 s33, 8
	s_nop 0
	v_writelane_b32 v252, s1, 53
	s_cselect_b64 s[0:1], -1, 0
	v_writelane_b32 v252, s0, 54
	s_cmp_eq_u32 s33, 7
	s_nop 0
	v_writelane_b32 v252, s1, 55
	s_cselect_b64 s[0:1], -1, 0
	v_writelane_b32 v252, s0, 56
	s_cmp_eq_u32 s33, 6
	s_nop 0
	v_writelane_b32 v252, s1, 57
	s_cselect_b64 s[0:1], -1, 0
	v_writelane_b32 v252, s0, 58
	s_cmp_eq_u32 s33, 5
	s_nop 0
	v_writelane_b32 v252, s1, 59
	s_cselect_b64 s[0:1], -1, 0
	v_writelane_b32 v252, s0, 60
	s_cmp_eq_u32 s33, 4
	s_nop 0
	v_writelane_b32 v252, s1, 61
	s_cselect_b64 s[0:1], -1, 0
	v_writelane_b32 v252, s0, 62
	s_cmp_eq_u32 s33, 3
	s_nop 0
	v_writelane_b32 v252, s1, 63
	s_cselect_b64 s[0:1], -1, 0
	v_writelane_b32 v253, s0, 0
	s_cmp_eq_u32 s33, 2
	s_nop 0
	v_writelane_b32 v253, s1, 1
	s_cselect_b64 s[0:1], -1, 0
	v_writelane_b32 v253, s0, 2
	s_cmp_eq_u32 s33, 1
	s_nop 0
	v_writelane_b32 v253, s1, 3
	s_cselect_b64 s[0:1], -1, 0
	v_writelane_b32 v253, s0, 4
	s_cmp_eq_u32 s33, 0
	s_nop 0
	v_writelane_b32 v253, s1, 5
	s_cselect_b64 s[0:1], -1, 0
	v_writelane_b32 v253, s0, 6
	s_nop 1
	v_writelane_b32 v253, s1, 7
	s_lshl_b32 s0, s33, 8
	s_add_u32 s0, s14, s0
	s_addc_u32 s1, s15, 0
	s_add_u32 s6, s0, 0x1400
	s_addc_u32 s7, s1, 0
	v_writelane_b32 v253, s6, 8
	s_add_u32 s0, s0, 0x2400
	s_addc_u32 s1, s1, 0
	v_writelane_b32 v253, s7, 9
	v_writelane_b32 v253, s0, 10
	s_nop 1
	v_writelane_b32 v253, s1, 11
	s_add_u32 s0, s16, 0x7400
	s_addc_u32 s1, s17, 0
	v_writelane_b32 v253, s0, 12
	s_nop 1
	v_writelane_b32 v253, s1, 13
	s_add_u32 s0, s16, 0x7500
	s_addc_u32 s1, s17, 0
	v_writelane_b32 v253, s0, 14
	s_nop 1
	v_writelane_b32 v253, s1, 15
	s_add_u32 s0, s16, 0x1a10aa00
	s_addc_u32 s1, s17, 0
	v_writelane_b32 v253, s0, 16
	s_nop 1
	v_writelane_b32 v253, s1, 17
	s_add_u32 s0, s16, 0x1a50bb00
	s_addc_u32 s1, s17, 0
	v_writelane_b32 v253, s0, 18
	s_cmpk_lt_i32 s96, 0x100
	s_nop 0
	v_writelane_b32 v253, s1, 19
	s_cselect_b64 s[0:1], -1, 0
	v_writelane_b32 v253, s0, 20
	s_nop 1
	v_writelane_b32 v253, s1, 21
	s_add_u32 s0, s16, 0x16108800
	s_addc_u32 s1, s17, 0
	s_add_u32 s78, s16, 0x18109900
	s_addc_u32 s79, s17, 0
	s_add_u32 s5, s16, 0x26515400
	v_writelane_b32 v253, s5, 22
	s_addc_u32 s5, s17, 0
	s_add_u32 s6, s16, 0x16108880
	v_writelane_b32 v253, s5, 23
	s_addc_u32 s7, s17, 0
	s_add_i32 s5, s20, 0xffffff78
	v_writelane_b32 v253, s6, 24
	s_cmp_lt_i32 s66, s5
	s_nop 0
	v_writelane_b32 v253, s7, 25
	s_cselect_b64 s[6:7], -1, 0
	v_writelane_b32 v253, s6, 26
	s_nop 1
	v_writelane_b32 v253, s7, 27
	v_writelane_b32 v253, s5, 28
	s_sub_i32 s5, s66, s5
	s_lshl_b32 s6, s5, 3
	v_writelane_b32 v253, s6, 29
	s_add_u32 s6, s16, 0x20311000
	v_writelane_b32 v253, s6, 30
	s_addc_u32 s6, s17, 0
	v_writelane_b32 v253, s6, 31
	s_add_u32 s6, s16, 0x24312100
	v_writelane_b32 v253, s6, 32
	s_addc_u32 s6, s17, 0
	v_writelane_b32 v253, s6, 33
	s_add_u32 s6, s16, 0x27516500
	v_writelane_b32 v253, s6, 34
	s_addc_u32 s6, s17, 0
	v_writelane_b32 v253, s6, 35
	s_add_u32 s6, s16, 0x47517600
	v_writelane_b32 v253, s6, 36
	s_addc_u32 s6, s17, 0
	v_writelane_b32 v253, s6, 37
	s_add_u32 s6, s16, 0x5f61ba00
	s_addc_u32 s7, s17, 0
	v_writelane_b32 v253, s6, 38
	s_lshl_b32 s5, s5, 9
	s_cmpk_lt_i32 s66, 0x400
	v_writelane_b32 v253, s7, 39
	v_writelane_b32 v253, s5, 40
	s_cselect_b64 s[6:7], -1, 0
	v_writelane_b32 v253, s6, 41
	s_lshl_b32 s5, s3, 7
	s_nop 0
	v_writelane_b32 v253, s7, 42
	s_add_u32 s6, s16, 0x8103300
	s_addc_u32 s7, s17, 0
	s_add_u32 s10, s16, 0xa104400
	v_writelane_b32 v253, s6, 43
	s_addc_u32 s11, s17, 0
	s_nop 0
	v_writelane_b32 v253, s7, 44
	s_add_u32 s6, s16, 0x12107700
	s_addc_u32 s7, s17, 0
	v_writelane_b32 v253, s6, 45
	s_nop 1
	v_writelane_b32 v253, s7, 46
	s_add_u32 s6, s16, 0x57518700
	s_addc_u32 s7, s17, 0
	v_writelane_b32 v253, s6, 47
	s_nop 1
	v_writelane_b32 v253, s7, 48
	s_add_u32 s6, s16, 0x5f51a900
	s_addc_u32 s7, s17, 0
	v_writelane_b32 v253, s6, 49
	s_cmpk_lt_i32 s96, 0x800
	s_nop 0
	v_writelane_b32 v253, s7, 50
	s_cselect_b64 s[6:7], -1, 0
	v_writelane_b32 v253, s6, 51
	s_lshl_b32 s9, s96, 13
	s_and_b32 s9, s9, 0x3e0000
	v_writelane_b32 v253, s7, 52
	s_lshl_b32 s6, s96, 7
	s_and_b32 s8, s6, 0x780
	s_ashr_i32 s6, s96, 9
	s_ashr_i32 s7, s6, 31
	s_lshl_b64 s[6:7], s[6:7], 22
	s_or_b32 s6, s6, s9
	s_or_b32 s6, s6, s8
	v_writelane_b32 v253, s6, 53
	s_nop 1
	v_writelane_b32 v253, s7, 54
	s_lshl_b64 s[6:7], s[6:7], 1
	v_writelane_b32 v253, s10, 55
	s_add_u32 s6, s10, s6
	v_writelane_b32 v253, s11, 56
	s_addc_u32 s7, s11, s7
	v_writelane_b32 v253, s6, 57
	s_nop 1
	v_writelane_b32 v253, s7, 58
	s_add_u32 s6, s16, 0x5b519800
	s_addc_u32 s7, s17, 0
	v_writelane_b32 v253, s6, 59
	s_nop 1
	v_writelane_b32 v253, s7, 60
	s_lshl_b32 s6, s96, 9
	v_writelane_b32 v253, s6, 61
	s_lshl_b32 s6, s20, 9
	v_writelane_b32 v253, s6, 62
	s_add_u32 s6, s16, 0xc105500
	s_addc_u32 s7, s17, 0
	v_writelane_b32 v253, s6, 63
	s_cmpk_lt_i32 s96, 0x400
	s_nop 0
	v_writelane_b32 v254, s7, 0
	s_cselect_b64 s[6:7], -1, 0
	v_writelane_b32 v254, s6, 1
	s_nop 1
	v_writelane_b32 v254, s7, 2
	s_lshl_b32 s6, s96, 4
	v_writelane_b32 v254, s6, 3
	s_and_b32 s6, s6, 0xf0
	s_and_b32 s7, s96, 0x7fffff00
	s_or_b32 s6, s7, s6
	s_bfe_u32 s7, s96, 0x40004
	s_or_b32 s6, s6, s7
	s_lshl_b32 s6, s6, 1
	s_add_u32 s22, s16, 0x4101100
	s_addc_u32 s23, s17, 0
	v_writelane_b32 v254, s6, 4
	s_add_u32 s6, s16, 0x6381dc00
	s_addc_u32 s7, s17, 0
	v_writelane_b32 v254, s6, 5
	s_nop 1
	v_writelane_b32 v254, s7, 6
	s_add_u32 s6, s16, 0x1a90cc00
	s_addc_u32 s7, s17, 0
	v_writelane_b32 v254, s6, 7
	s_nop 1
	v_writelane_b32 v254, s7, 8
	s_add_u32 s6, s16, 0x1aa0dd00
	s_addc_u32 s7, s17, 0
	v_writelane_b32 v254, s6, 9
	s_lshl_b32 s8, s96, 5
	s_nop 0
	v_writelane_b32 v254, s7, 10
	s_ashr_i32 s6, s20, 31
	s_lshr_b32 s6, s6, 30
	s_add_i32 s6, s20, s6
	s_ashr_i32 s6, s6, 2
	v_writelane_b32 v254, s6, 11
	s_add_u32 s6, s16, 0x10000
	v_writelane_b32 v254, s6, 12
	s_addc_u32 s6, s17, 0
	s_lshl_b32 s7, s20, 1
	v_writelane_b32 v254, s6, 13
	s_add_i32 s9, s96, s7
	v_writelane_b32 v254, s7, 14
	s_ashr_i32 s7, s9, 31
	s_ashr_i32 s6, s96, 31
	s_lshr_b32 s7, s7, 30
	s_lshr_b32 s6, s6, 30
	s_add_i32 s7, s9, s7
	s_add_i32 s6, s96, s6
	v_writelane_b32 v254, s9, 15
	s_ashr_i32 s7, s7, 2
	v_writelane_b32 v254, s7, 16
	s_ashr_i32 s7, s6, 2
	s_add_u32 s24, s16, 0x1ab0ee00
	s_addc_u32 s25, s17, 0
	s_add_u32 s10, s16, 0x6391ed00
	v_writelane_b32 v254, s7, 17
	s_addc_u32 s11, s17, 0
	v_writelane_b32 v254, s10, 18
	s_and_b32 s6, s6, -4
	s_sub_i32 s6, s96, s6
	v_writelane_b32 v254, s11, 19
	v_writelane_b32 v254, s6, 20
	s_add_u32 s6, s16, 0x4101180
	s_addc_u32 s7, s17, 0
	v_writelane_b32 v254, s6, 21
	s_nop 1
	v_writelane_b32 v254, s7, 22
	s_add_u32 s6, s16, 0x1c30ff00
	s_addc_u32 s7, s17, 0
	v_writelane_b32 v254, s6, 23
	s_nop 1
	v_writelane_b32 v254, s7, 24
	s_add_u32 s6, s16, 0x1ab0ee80
	s_addc_u32 s7, s17, 0
	v_writelane_b32 v254, s6, 25
	s_nop 1
	v_writelane_b32 v254, s7, 26
	s_add_u32 s6, s16, 0x1e310780
	s_addc_u32 s7, s17, 0
	v_writelane_b32 v254, s6, 27
	s_cmp_lt_i32 s3, 0
	s_nop 0
	v_writelane_b32 v254, s7, 28
	s_mul_i32 s6, s3, 33
	s_cselect_b32 s4, s6, s4
	s_mulk_i32 s3, 0x81
	s_cselect_b32 s3, s3, s5
	s_add_i32 s4, s4, s2
	s_ashr_i32 s5, s4, 31
	s_lshr_b32 s5, s5, 26
	s_add_i32 s5, s4, s5
	s_and_b32 s6, s5, 0xffc0
	s_sub_i32 s4, s4, s6
	s_bfe_i32 s6, s4, 0x80000
	s_bfe_u32 s6, s6, 0x3000c
	s_add_i32 s6, s4, s6
	s_and_b32 s7, s6, 0xf8
	s_add_i32 s2, s3, s2
	s_sub_i32 s4, s4, s7
	s_ashr_i32 s3, s2, 31
	s_sext_i32_i8 s4, s4
	s_lshl_b32 s5, s5, 5
	s_lshr_b32 s3, s3, 24
	s_and_b32 s5, s5, 0xfffff800
	s_lshl_b32 s4, s4, 8
	s_add_i32 s3, s2, s3
	s_add_i32 s7, s4, s5
	s_and_b32 s4, s3, 0xff00
	s_sub_i32 s2, s2, s4
	s_sext_i32_i16 s4, s2
	s_bfe_u32 s4, s4, 0x3001c
	s_add_i32 s4, s2, s4
	s_and_b32 s5, s4, 0xfff8
	s_sub_i32 s2, s2, s5
	s_sext_i32_i16 s2, s2
	s_lshl_b32 s3, s3, 3
	s_and_b32 s3, s3, 0xfffff800
	s_lshl_b32 s2, s2, 8
	s_add_i32 s5, s2, s3
	s_bfe_i32 s2, s6, 0x80000
	s_sext_i32_i16 s2, s2
	s_ashr_i32 s3, s2, 3
	s_lshr_b32 s2, s2, 3
	v_writelane_b32 v254, s3, 29
	s_bfe_i64 s[2:3], s[2:3], 0x100000
	s_lshl_b64 s[2:3], s[2:3], 20
	v_writelane_b32 v254, s2, 30
	s_nop 1
	v_writelane_b32 v254, s3, 31
	s_sext_i32_i16 s2, s4
	s_ashr_i32 s3, s2, 3
	s_lshr_b32 s2, s2, 3
	v_writelane_b32 v254, s3, 32
	s_bfe_i64 s[2:3], s[2:3], 0x100000
	s_lshl_b64 s[2:3], s[2:3], 20
	v_writelane_b32 v254, s2, 33
	s_nop 1
	v_writelane_b32 v254, s3, 34
	v_writelane_b32 v254, s7, 35
	s_or_b32 s2, s7, 0x80
	v_writelane_b32 v254, s2, 36
	v_writelane_b32 v254, s5, 37
	s_or_b32 s2, s5, 0x80
	v_writelane_b32 v254, s2, 38
	s_lshl_b32 s2, s20, 5
	v_writelane_b32 v254, s2, 39
	s_lshl_b32 s2, s96, 12
	v_writelane_b32 v254, s2, 40
	s_lshl_b32 s2, s20, 12
	v_writelane_b32 v254, s2, 41
	s_lshl_b32 s2, s20, 4
	v_writelane_b32 v254, s2, 42
	v_writelane_b32 v254, s8, 43
	s_or_b32 s2, s8, 1
	v_writelane_b32 v254, s2, 44
	s_add_u32 s2, s16, 0x100c00
	s_addc_u32 s3, s17, 0
	v_writelane_b32 v254, s2, 45
	s_ashr_i32 s89, s88, 31
	s_nop 0
	v_writelane_b32 v254, s3, 46
	v_readlane_b32 s2, v251, 29
	v_readlane_b32 s3, v251, 30
	s_ashr_i32 s3, s2, 31
	v_writelane_b32 v251, s2, 29
	s_nop 1
	v_writelane_b32 v251, s3, 30
	s_mov_b32 s2, 1
	v_writelane_b32 v254, s2, 47
	s_add_i32 s2, 0, 0x19a00
	v_writelane_b32 v254, s2, 48
	s_add_i32 s2, 0, 0x13200
	v_writelane_b32 v254, s2, 49
	s_add_i32 s2, 0, 0x17600
	v_writelane_b32 v254, s2, 50
	s_add_i32 s2, 0, 0x20080
	v_writelane_b32 v254, s2, 51
	s_add_i32 s2, 0, 0x20120
	v_writelane_b32 v254, s2, 52
	s_add_i32 s2, 0, 0x201c0
	v_writelane_b32 v254, s2, 53
	v_cmp_eq_u32_e64 s[2:3], 0, v0
	s_nop 1
	v_writelane_b32 v254, s2, 54
	s_nop 1
	v_writelane_b32 v254, s3, 55
	s_lshl_b64 s[2:3], s[88:89], 12
	v_writelane_b32 v254, s2, 56
	s_nop 1
	v_writelane_b32 v254, s3, 57
	s_lshl_b64 s[2:3], s[88:89], 13
	v_writelane_b32 v254, s2, 58
	s_nop 1
	v_writelane_b32 v254, s3, 59
	s_mov_b64 s[2:3], s[16:17]
	v_writelane_b32 v254, s2, 60
	s_nop 1
	v_writelane_b32 v254, s3, 61
	v_writelane_b32 v254, s66, 62
	s_mov_b32 s2, s88
	v_writelane_b32 v254, s2, 63
	s_nop 1
	v_writelane_b32 v250, s3, 0
	v_writelane_b32 v250, s78, 1
	s_nop 1
	v_writelane_b32 v250, s79, 2
	v_writelane_b32 v250, s96, 3
	s_nop 1
	v_writelane_b32 v250, s97, 4
	v_writelane_b32 v250, s26, 5
	s_nop 1
	v_writelane_b32 v250, s27, 6
	s_branch .LBB0_106

.LBB0_387:
	v_lshlrev_b32_e32 v2, 3, v38
	s_mulk_i32 s5, 0x2100
	v_lshrrev_b32_e32 v40, 3, v38
	v_and_b32_e32 v2, 56, v2
	s_add_i32 s5, s5, 0
	v_lshrrev_b32_e32 v37, 5, v38
	v_and_b32_e32 v36, 31, v1
	v_mul_u32_u24_e32 v38, 0x84, v2
	v_lshlrev_b32_e32 v41, 2, v40
	v_lshl_add_u32 v39, v36, 2, s5
	v_mul_u32_u24_e32 v45, 0x84, v37
	v_add3_u32 v41, s5, v38, v41
	s_lshl_b32 s5, s33, 6
	v_or_b32_e32 v42, 8, v40
	v_or_b32_e32 v43, 16, v40
	v_or_b32_e32 v44, 24, v40
	s_lshl_b32 s52, s33, 5
	s_add_i32 s53, s5, 0x22000
	v_lshlrev_b32_e32 v38, 1, v2
	v_add_u32_e32 v45, v39, v45
	s_branch .LBB0_389
.LBB0_388:
	s_add_i32 s52, s52, 0x11000
	s_add_i32 s53, s53, 0x22000
	s_andn2_b64 vcc, exec, s[40:41]
	s_mov_b32 s33, s5
	s_cbranch_vccz .LBB0_443
.LBB0_389:
	s_cmp_lt_i32 s33, 0x36dc0
	s_cselect_b64 s[38:39], -1, 0
	s_cmp_gt_i32 s33, 0x36dbf
	s_cbranch_scc1 .LBB0_414
	s_add_i32 s5, s33, 0x440
	s_cmpk_gt_i32 s33, 0x3bbf
	s_mov_b64 s[48:49], -1
	s_cbranch_scc0 .LBB0_411
	s_cmpk_gt_u32 s5, 0x4fff
	s_cbranch_scc0 .LBB0_408
	s_cmpk_gt_u32 s5, 0x51ff
	s_cbranch_scc0 .LBB0_405
	s_cmpk_gt_u32 s5, 0x61ff
	s_cbranch_scc0 .LBB0_402
	s_cmpk_gt_u32 s5, 0x71ff
	s_cbranch_scc0 .LBB0_399
	s_cmp_gt_u32 s5, 0x271ff
	s_mov_b64 s[14:15], -1
	s_cbranch_scc0 .LBB0_397
	s_add_i32 s9, s33, 0xfffd9240
	s_lshr_b32 s34, s9, 9
	s_bfe_u32 s10, s5, 0x30006
	s_lshl_b64 s[12:13], s[34:35], 22
	v_readlane_b32 s56, v251, 0
	v_readlane_b32 s57, v251, 1
	s_add_u32 s40, s56, s12
	s_addc_u32 s41, s57, s13
	s_lshl_b64 s[12:13], s[34:35], 21
	v_readlane_b32 s9, v253, 36
	s_add_u32 s12, s9, s12
	v_readlane_b32 s9, v253, 37
	s_addc_u32 s13, s9, s13
	s_add_i32 s9, s52, 0x8800
	v_readlane_b32 s58, v251, 2
	v_readlane_b32 s59, v251, 3
	v_readlane_b32 s60, v251, 4
	v_readlane_b32 s61, v251, 5
	v_readlane_b32 s62, v251, 6
	v_readlane_b32 s63, v251, 7
	s_and_b32 s54, s9, 0x7e0
	s_mov_b64 s[14:15], 0
.LBB0_397:
	s_andn2_b64 vcc, exec, s[14:15]
	s_cbranch_vccnz .LBB0_441
	s_cmp_gt_u32 s5, 0x171ff
	s_cselect_b64 s[12:13], -1, 0
	s_and_b64 s[10:11], s[12:13], exec
	s_mov_b32 s10, 0xfffe8e00
	s_cselect_b32 s9, 0x80, 0
	s_cselect_b32 s10, s10, 0xffff8e00
	s_add_i32 s11, s52, 0x8800
	s_add_i32 s14, s53, 0xfffef000
	s_add_i32 s10, s10, s33
	s_and_b32 s14, s14, 0x300
	s_and_b32 s15, s11, 0x60
	s_addk_i32 s10, 0x440
	s_or_b32 s14, s14, s15
	s_lshr_b32 s34, s10, 9
	s_bfe_u32 s10, s5, 0x50004
	s_or_b32 s54, s14, s9
	v_readlane_b32 s68, v251, 31
	s_and_b64 s[12:13], s[12:13], exec
	v_readlane_b32 s80, v251, 43
	v_readlane_b32 s81, v251, 44
	v_readlane_b32 s82, v251, 45
	v_readlane_b32 s83, v251, 46
	s_cselect_b32 s9, s83, s81
	s_cselect_b32 s14, s82, s80
	s_lshl_b64 s[12:13], s[34:35], 22
	s_add_u32 s40, s14, s12
	v_readlane_b32 s78, v251, 41
	v_readlane_b32 s79, v251, 42
	s_addc_u32 s41, s9, s13
	v_readlane_b32 s9, v253, 34
	v_readlane_b32 s78, v250, 1
	s_add_u32 s12, s9, s12
	v_readlane_b32 s9, v253, 35
	v_readlane_b32 s69, v251, 32
	v_readlane_b32 s70, v251, 33
	v_readlane_b32 s71, v251, 34
	v_readlane_b32 s72, v251, 35
	v_readlane_b32 s73, v251, 36
	v_readlane_b32 s74, v251, 37
	v_readlane_b32 s75, v251, 38
	v_readlane_b32 s76, v251, 39
	v_readlane_b32 s77, v251, 40
	v_readlane_b32 s79, v250, 2
	s_addc_u32 s13, s9, s13
	s_and_b32 s44, s11, 0x1e0
	s_mov_b64 s[42:43], 0x200
	s_movk_i32 s14, 0x800
	s_mov_b64 s[48:49], 0

.LBB0_400:
	s_add_i32 s9, s33, 0xffffa240
	s_and_b32 s34, s9, 0xfffff800
	s_bfe_u32 s10, s9, 0x50006
	s_lshl_b64 s[12:13], s[34:35], 13
	v_readlane_b32 s68, v251, 31
	v_readlane_b32 s69, v251, 32
	s_add_u32 s40, s68, s12
	s_addc_u32 s41, s69, s13
	s_lshl_b64 s[12:13], s[34:35], 12
	v_readlane_b32 s9, v253, 22
	s_add_u32 s12, s9, s12
	v_readlane_b32 s9, v253, 23
	v_readlane_b32 s78, v251, 41
	v_readlane_b32 s79, v251, 42
	s_addc_u32 s13, s9, s13
	s_add_i32 s9, s52, 0x8800
	v_readlane_b32 s78, v250, 1
	s_and_b32 s54, s9, 0x7e0
	v_readlane_b32 s79, v250, 2
	s_mov_b64 s[42:43], 0x800
	s_movk_i32 s14, 0x800
	s_mov_b32 s44, s54
	v_readlane_b32 s70, v251, 33
	v_readlane_b32 s71, v251, 34
	v_readlane_b32 s72, v251, 35
	v_readlane_b32 s73, v251, 36
	v_readlane_b32 s74, v251, 37
	v_readlane_b32 s75, v251, 38
	v_readlane_b32 s76, v251, 39
	v_readlane_b32 s77, v251, 40
	v_readlane_b32 s80, v251, 43
	v_readlane_b32 s81, v251, 44
	v_readlane_b32 s82, v251, 45
	v_readlane_b32 s83, v251, 46

.LBB0_402:
	s_andn2_b64 vcc, exec, s[48:49]
	s_cbranch_vccnz .LBB0_404
	s_add_i32 s9, s33, 0xffffb240
	s_and_b32 s34, s9, 0xfffff800
	v_readlane_b32 s68, v251, 12
	s_bfe_u32 s10, s9, 0x50006
	s_lshl_b64 s[12:13], s[34:35], 13
	v_readlane_b32 s80, v251, 24
	v_readlane_b32 s81, v251, 25
	s_add_u32 s40, s80, s12
	s_addc_u32 s41, s81, s13
	s_lshl_b64 s[12:13], s[34:35], 12
	v_readlane_b32 s9, v252, 1
	s_add_u32 s12, s9, s12
	v_readlane_b32 s9, v252, 2
	v_readlane_b32 s78, v251, 22
	v_readlane_b32 s79, v251, 23
	s_addc_u32 s13, s9, s13
	s_add_i32 s9, s52, 0x8800
	v_readlane_b32 s78, v250, 1
	s_and_b32 s54, s9, 0x7e0
	v_readlane_b32 s79, v250, 2
	s_mov_b64 s[42:43], 0x800
	s_movk_i32 s14, 0x800
	s_mov_b32 s44, s54
	v_readlane_b32 s69, v251, 13
	v_readlane_b32 s70, v251, 14
	v_readlane_b32 s71, v251, 15
	v_readlane_b32 s72, v251, 16
	v_readlane_b32 s73, v251, 17
	v_readlane_b32 s74, v251, 18
	v_readlane_b32 s75, v251, 19
	v_readlane_b32 s76, v251, 20
	v_readlane_b32 s77, v251, 21
	v_readlane_b32 s82, v251, 26
	v_readlane_b32 s83, v251, 27

.LBB0_406:
	s_add_i32 s9, s33, 0xffffb440
	s_lshr_b32 s10, s9, 4
	s_add_i32 s9, s52, 0x8800
	s_and_b32 s54, s9, 0x1e0
	s_mov_b64 s[42:43], 0x200
	s_movk_i32 s14, 0x800
	s_mov_b64 s[12:13], s[26:27]
	s_mov_b32 s44, s54

.LBB0_408:
	s_andn2_b64 vcc, exec, s[48:49]
	s_cbranch_vccnz .LBB0_410
	s_and_b32 s9, s5, 0x7800
	s_add_i32 s34, s9, 0xffffc000
	v_readlane_b32 s68, v251, 12
	s_bfe_u32 s10, s5, 0x50006
	s_lshl_b64 s[12:13], s[34:35], 13
	v_readlane_b32 s76, v251, 20
	v_readlane_b32 s77, v251, 21
	s_add_u32 s40, s76, s12
	s_addc_u32 s41, s77, s13
	s_lshl_b64 s[12:13], s[34:35], 12
	v_readlane_b32 s9, v253, 32
	s_add_u32 s12, s9, s12
	v_readlane_b32 s9, v253, 33
	v_readlane_b32 s78, v251, 22
	v_readlane_b32 s79, v251, 23
	s_addc_u32 s13, s9, s13
	s_add_i32 s9, s52, 0x8800
	v_readlane_b32 s78, v250, 1
	s_and_b32 s54, s9, 0x7e0
	v_readlane_b32 s79, v250, 2
	s_mov_b64 s[42:43], 0x800
	s_movk_i32 s14, 0x800
	s_mov_b32 s44, s54
	v_readlane_b32 s69, v251, 13
	v_readlane_b32 s70, v251, 14
	v_readlane_b32 s71, v251, 15
	v_readlane_b32 s72, v251, 16
	v_readlane_b32 s73, v251, 17
	v_readlane_b32 s74, v251, 18
	v_readlane_b32 s75, v251, 19
	v_readlane_b32 s80, v251, 24
	v_readlane_b32 s81, v251, 25
	v_readlane_b32 s82, v251, 26
	v_readlane_b32 s83, v251, 27

.Lcv_join_a:
	v_add_u32_e32 v78, 0x400, v45
	v_add_u32_e32 v79, 0x800, v45
	v_add_u32_e32 v80, 0xc00, v45
	v_add_u32_e32 v81, 0x1000, v45
	v_add_u32_e32 v82, 0x1400, v45
	v_add_u32_e32 v83, 0x1800, v45
	v_add_u32_e32 v88, 0x1c00, v45
	ds_write2_b32 v45, v4, v5 offset1:66
	ds_write2_b32 v45, v6, v7 offset0:132 offset1:198
	ds_write2_b32 v78, v8, v9 offset0:8 offset1:74
	ds_write2_b32 v78, v10, v11 offset0:140 offset1:206
	ds_write2_b32 v79, v12, v13 offset0:16 offset1:82
	ds_write2_b32 v79, v14, v15 offset0:148 offset1:214
	ds_write2_b32 v80, v16, v17 offset0:24 offset1:90
	ds_write2_b32 v80, v18, v19 offset0:156 offset1:222
	ds_write2_b32 v81, v20, v21 offset0:32 offset1:98
	ds_write2_b32 v81, v22, v23 offset0:164 offset1:230
	ds_write2_b32 v82, v24, v25 offset0:40 offset1:106
	ds_write2_b32 v82, v26, v27 offset0:172 offset1:238
	ds_write2_b32 v83, v28, v29 offset0:48 offset1:114
	ds_write2_b32 v83, v30, v31 offset0:180 offset1:246
	ds_write2_b32 v88, v32, v33 offset0:56 offset1:122
	ds_write2_b32 v88, v34, v35 offset0:188 offset1:254
	v_add_u32_e32 v2, s47, v40
	s_waitcnt lgkmcnt(0)
	v_ashrrev_i32_e32 v39, 8, v2
	s_ashr_i32 s9, s8, 31
	ds_read2_b32 v[94:95], v41 offset0:33 offset1:41
	ds_read2_b32 v[96:97], v41 offset1:8
	ds_read2_b32 v[98:99], v41 offset0:66 offset1:74
	ds_read2_b32 v[100:101], v41 offset0:99 offset1:107
	ds_read2_b32 v[102:103], v41 offset0:132 offset1:140
	ds_read2_b32 v[104:105], v41 offset0:165 offset1:173
	ds_read2_b32 v[106:107], v41 offset0:198 offset1:206
	ds_read2_b32 v[108:109], v41 offset0:231 offset1:239
	v_ashrrev_i32_e32 v89, 31, v39
	s_lshl_b32 s11, s8, 8
	s_lshr_b64 s[40:41], s[8:9], 24
	s_waitcnt lgkmcnt(0)
	v_cvt_pk_bf16_f32 v90, v96, v94
	v_mul_lo_u32 v94, s40, v39
	v_mul_lo_u32 v89, s11, v89
	v_mad_u64_u32 v[110:111], s[42:43], s11, v39, 0
	v_add3_u32 v111, v111, v89, v94
	s_ashr_i32 s5, s4, 31
	v_lshl_add_u64 v[110:111], v[110:111], 1, s[6:7]
	s_lshl_b64 s[42:43], s[4:5], 15
	v_lshlrev_b32_e32 v2, 7, v2
	v_lshl_add_u64 v[110:111], v[110:111], 0, s[42:43]
	v_and_b32_e32 v2, 0x7f80, v2
	v_lshl_add_u64 v[110:111], v[110:111], 0, v[2:3]
	v_add_u32_e32 v2, s47, v42
	v_mov_b32_e32 v39, v3
	v_ashrrev_i32_e32 v89, 8, v2
	v_cvt_pk_bf16_f32 v91, v98, v100
	v_cvt_pk_bf16_f32 v92, v102, v104
	v_cvt_pk_bf16_f32 v93, v106, v108
	v_lshl_add_u64 v[110:111], v[110:111], 0, v[38:39]
	v_ashrrev_i32_e32 v94, 31, v89
	global_store_dwordx4 v[110:111], v[90:93], off nt
	v_mul_lo_u32 v96, s40, v89
	v_lshlrev_b32_e32 v2, 7, v2
	v_cvt_pk_bf16_f32 v90, v97, v95
	v_mul_lo_u32 v97, s11, v94
	v_mad_u64_u32 v[94:95], s[44:45], s11, v89, 0
	v_add3_u32 v95, v95, v97, v96
	v_lshl_add_u64 v[94:95], v[94:95], 1, s[6:7]
	v_lshl_add_u64 v[94:95], v[94:95], 0, s[42:43]
	v_and_b32_e32 v2, 0x7f80, v2
	v_lshl_add_u64 v[94:95], v[94:95], 0, v[2:3]
	v_add_u32_e32 v2, s47, v43
	v_cvt_pk_bf16_f32 v91, v99, v101
	v_cvt_pk_bf16_f32 v92, v103, v105
	v_cvt_pk_bf16_f32 v93, v107, v109
	v_lshl_add_u64 v[94:95], v[94:95], 0, v[38:39]
	v_ashrrev_i32_e32 v89, 8, v2
	ds_read2_b32 v[96:97], v41 offset0:16 offset1:24
	ds_read2_b32 v[98:99], v41 offset0:49 offset1:57
	ds_read2_b32 v[100:101], v41 offset0:82 offset1:90
	ds_read2_b32 v[102:103], v41 offset0:115 offset1:123
	ds_read2_b32 v[104:105], v41 offset0:148 offset1:156
	ds_read2_b32 v[106:107], v41 offset0:181 offset1:189
	ds_read2_b32 v[108:109], v41 offset0:214 offset1:222
	ds_read2_b32 v[110:111], v41 offset0:247 offset1:255
	global_store_dwordx4 v[94:95], v[90:93], off nt
	v_ashrrev_i32_e32 v94, 31, v89
	v_lshlrev_b32_e32 v2, 7, v2
	s_waitcnt lgkmcnt(6)
	v_cvt_pk_bf16_f32 v90, v96, v98
	v_mul_lo_u32 v96, s40, v89
	v_mul_lo_u32 v98, s11, v94
	v_mad_u64_u32 v[94:95], s[44:45], s11, v89, 0
	v_add3_u32 v95, v95, v98, v96
	v_lshl_add_u64 v[94:95], v[94:95], 1, s[6:7]
	v_lshl_add_u64 v[94:95], v[94:95], 0, s[42:43]
	v_and_b32_e32 v2, 0x7f80, v2
	v_lshl_add_u64 v[94:95], v[94:95], 0, v[2:3]
	v_add_u32_e32 v2, s47, v44
	s_waitcnt lgkmcnt(4)
	v_cvt_pk_bf16_f32 v91, v100, v102
	s_waitcnt lgkmcnt(2)
	v_cvt_pk_bf16_f32 v92, v104, v106
	s_waitcnt lgkmcnt(0)
	v_cvt_pk_bf16_f32 v93, v108, v110
	v_lshl_add_u64 v[94:95], v[94:95], 0, v[38:39]
	v_ashrrev_i32_e32 v89, 8, v2
	global_store_dwordx4 v[94:95], v[90:93], off nt
	v_ashrrev_i32_e32 v94, 31, v89
	v_mul_lo_u32 v96, s40, v89
	v_cvt_pk_bf16_f32 v90, v97, v99
	v_mul_lo_u32 v97, s11, v94
	v_mad_u64_u32 v[94:95], s[40:41], s11, v89, 0
	v_add3_u32 v95, v95, v97, v96
	v_lshl_add_u64 v[94:95], v[94:95], 1, s[6:7]
	v_lshlrev_b32_e32 v2, 7, v2
	v_lshl_add_u64 v[94:95], v[94:95], 0, s[42:43]
	v_and_b32_e32 v2, 0x7f80, v2
	v_lshl_add_u64 v[94:95], v[94:95], 0, v[2:3]
	v_cvt_pk_bf16_f32 v91, v101, v103
	v_cvt_pk_bf16_f32 v92, v105, v107
	v_cvt_pk_bf16_f32 v93, v109, v111
	v_lshl_add_u64 v[94:95], v[94:95], 0, v[38:39]
	global_store_dwordx4 v[94:95], v[90:93], off nt
	s_add_i32 s5, s33, 0x880
	s_waitcnt lgkmcnt(0)
	s_cmp_gt_i32 s33, 0x3697f
	s_cselect_b64 s[40:41], -1, 0
	s_and_b64 vcc, exec, s[40:41]
	s_cbranch_vccnz .LBB0_439
	s_cmpk_gt_i32 s33, 0x377f
	s_mov_b64 s[50:51], -1
	s_cbranch_scc0 .LBB0_436
	s_cmpk_gt_u32 s5, 0x4fff
	s_cbranch_scc0 .LBB0_433
	s_cmpk_gt_u32 s5, 0x51ff
	s_cbranch_scc0 .LBB0_430
	s_cmpk_gt_u32 s5, 0x61ff
	s_cbranch_scc0 .LBB0_427
	s_cmpk_gt_u32 s5, 0x71ff
	s_cbranch_scc0 .LBB0_424
	s_cmp_gt_u32 s5, 0x271ff
	s_mov_b64 s[8:9], -1
	s_cbranch_scc0 .LBB0_422
	s_add_i32 s4, s33, 0xfffd9680
	s_lshr_b32 s34, s4, 9
	s_bfe_u32 s4, s5, 0x30006
	s_lshl_b64 s[6:7], s[34:35], 22
	v_readlane_b32 s56, v251, 0
	v_readlane_b32 s57, v251, 1
	s_add_u32 s42, s56, s6
	s_addc_u32 s43, s57, s7
	s_lshl_b64 s[6:7], s[34:35], 21
	v_readlane_b32 s8, v253, 36
	s_add_u32 s6, s8, s6
	v_readlane_b32 s8, v253, 37
	s_addc_u32 s7, s8, s7
	s_add_i32 s8, s52, 0x11000
	v_readlane_b32 s58, v251, 2
	v_readlane_b32 s59, v251, 3
	v_readlane_b32 s60, v251, 4
	v_readlane_b32 s61, v251, 5
	v_readlane_b32 s62, v251, 6
	v_readlane_b32 s63, v251, 7
	s_and_b32 s47, s8, 0x7e0
	s_mov_b64 s[8:9], 0
.LBB0_422:
	s_andn2_b64 vcc, exec, s[8:9]
	s_cbranch_vccnz .LBB0_442
	s_cmp_gt_u32 s5, 0x171ff
	s_cselect_b64 s[6:7], -1, 0
	s_and_b64 s[8:9], s[6:7], exec
	s_mov_b32 s4, 0xfffe8e00
	s_cselect_b32 s8, 0x80, 0
	s_cselect_b32 s4, s4, 0xffff8e00
	s_add_i32 s9, s52, 0x11000
	s_add_i32 s4, s4, s33
	s_and_b32 s11, s53, 0x300
	s_and_b32 s9, s9, 0x60
	s_addk_i32 s4, 0x880
	s_or_b32 s9, s11, s9
	s_lshr_b32 s34, s4, 9
	s_bfe_u32 s4, s5, 0x50004
	s_or_b32 s47, s9, s8
	v_readlane_b32 s68, v251, 31
	s_and_b64 s[6:7], s[6:7], exec
	v_readlane_b32 s80, v251, 43
	v_readlane_b32 s81, v251, 44
	v_readlane_b32 s82, v251, 45
	v_readlane_b32 s83, v251, 46
	s_cselect_b32 s8, s83, s81
	s_cselect_b32 s9, s82, s80
	s_lshl_b64 s[6:7], s[34:35], 22
	s_add_u32 s42, s9, s6
	v_readlane_b32 s78, v251, 41
	v_readlane_b32 s79, v251, 42
	s_addc_u32 s43, s8, s7
	v_readlane_b32 s8, v253, 34
	v_readlane_b32 s78, v250, 1
	s_add_u32 s6, s8, s6
	v_readlane_b32 s8, v253, 35
	v_readlane_b32 s69, v251, 32
	v_readlane_b32 s70, v251, 33
	v_readlane_b32 s71, v251, 34
	v_readlane_b32 s72, v251, 35
	v_readlane_b32 s73, v251, 36
	v_readlane_b32 s74, v251, 37
	v_readlane_b32 s75, v251, 38
	v_readlane_b32 s76, v251, 39
	v_readlane_b32 s77, v251, 40
	v_readlane_b32 s79, v250, 2
	s_addc_u32 s7, s8, s7
	s_and_b32 s48, s52, 0x1e0
	s_mov_b64 s[44:45], 0x200
	s_movk_i32 s8, 0x800
	s_mov_b64 s[50:51], 0

.LBB0_425:
	s_add_i32 s4, s33, 0xffffa680
	s_and_b32 s34, s4, 0xfffff800
	s_bfe_u32 s4, s4, 0x50006
	s_lshl_b64 s[6:7], s[34:35], 13
	v_readlane_b32 s68, v251, 31
	v_readlane_b32 s69, v251, 32
	s_add_u32 s42, s68, s6
	s_addc_u32 s43, s69, s7
	s_lshl_b64 s[6:7], s[34:35], 12
	v_readlane_b32 s8, v253, 22
	s_add_u32 s6, s8, s6
	v_readlane_b32 s8, v253, 23
	v_readlane_b32 s78, v251, 41
	v_readlane_b32 s79, v251, 42
	s_addc_u32 s7, s8, s7
	s_add_i32 s8, s52, 0x11000
	v_readlane_b32 s78, v250, 1
	s_and_b32 s47, s8, 0x7e0
	v_readlane_b32 s79, v250, 2
	s_mov_b64 s[44:45], 0x800
	s_movk_i32 s8, 0x800
	s_mov_b32 s48, s47
	v_readlane_b32 s70, v251, 33
	v_readlane_b32 s71, v251, 34
	v_readlane_b32 s72, v251, 35
	v_readlane_b32 s73, v251, 36
	v_readlane_b32 s74, v251, 37
	v_readlane_b32 s75, v251, 38
	v_readlane_b32 s76, v251, 39
	v_readlane_b32 s77, v251, 40
	v_readlane_b32 s80, v251, 43
	v_readlane_b32 s81, v251, 44
	v_readlane_b32 s82, v251, 45
	v_readlane_b32 s83, v251, 46

.LBB0_427:
	s_andn2_b64 vcc, exec, s[50:51]
	s_cbranch_vccnz .LBB0_429
	s_add_i32 s4, s33, 0xffffb680
	s_and_b32 s34, s4, 0xfffff800
	v_readlane_b32 s68, v251, 12
	s_bfe_u32 s4, s4, 0x50006
	s_lshl_b64 s[6:7], s[34:35], 13
	v_readlane_b32 s80, v251, 24
	v_readlane_b32 s81, v251, 25
	s_add_u32 s42, s80, s6
	s_addc_u32 s43, s81, s7
	s_lshl_b64 s[6:7], s[34:35], 12
	v_readlane_b32 s8, v252, 1
	s_add_u32 s6, s8, s6
	v_readlane_b32 s8, v252, 2
	v_readlane_b32 s78, v251, 22
	v_readlane_b32 s79, v251, 23
	s_addc_u32 s7, s8, s7
	s_add_i32 s8, s52, 0x11000
	v_readlane_b32 s78, v250, 1
	s_and_b32 s47, s8, 0x7e0
	v_readlane_b32 s79, v250, 2
	s_mov_b64 s[44:45], 0x800
	s_movk_i32 s8, 0x800
	s_mov_b32 s48, s47
	v_readlane_b32 s69, v251, 13
	v_readlane_b32 s70, v251, 14
	v_readlane_b32 s71, v251, 15
	v_readlane_b32 s72, v251, 16
	v_readlane_b32 s73, v251, 17
	v_readlane_b32 s74, v251, 18
	v_readlane_b32 s75, v251, 19
	v_readlane_b32 s76, v251, 20
	v_readlane_b32 s77, v251, 21
	v_readlane_b32 s82, v251, 26
	v_readlane_b32 s83, v251, 27

.LBB0_431:
	s_add_i32 s4, s33, 0xffffb880
	s_and_b32 s47, s52, 0x1e0
	s_lshr_b32 s4, s4, 4
	s_mov_b64 s[44:45], 0x200
	s_movk_i32 s8, 0x800
	s_mov_b64 s[6:7], s[26:27]
	s_mov_b32 s48, s47

.LBB0_433:
	s_andn2_b64 vcc, exec, s[50:51]
	s_cbranch_vccnz .LBB0_435
	s_and_b32 s4, s5, 0x7800
	s_add_i32 s34, s4, 0xffffc000
	v_readlane_b32 s68, v251, 12
	s_bfe_u32 s4, s5, 0x50006
	s_lshl_b64 s[6:7], s[34:35], 13
	v_readlane_b32 s76, v251, 20
	v_readlane_b32 s77, v251, 21
	s_add_u32 s42, s76, s6
	s_addc_u32 s43, s77, s7
	s_lshl_b64 s[6:7], s[34:35], 12
	v_readlane_b32 s8, v253, 32
	s_add_u32 s6, s8, s6
	v_readlane_b32 s8, v253, 33
	v_readlane_b32 s78, v251, 22
	v_readlane_b32 s79, v251, 23
	s_addc_u32 s7, s8, s7
	s_add_i32 s8, s52, 0x11000
	v_readlane_b32 s78, v250, 1
	s_and_b32 s47, s8, 0x7e0
	v_readlane_b32 s79, v250, 2
	s_mov_b64 s[44:45], 0x800
	s_movk_i32 s8, 0x800
	s_mov_b32 s48, s47
	v_readlane_b32 s69, v251, 13
	v_readlane_b32 s70, v251, 14
	v_readlane_b32 s71, v251, 15
	v_readlane_b32 s72, v251, 16
	v_readlane_b32 s73, v251, 17
	v_readlane_b32 s74, v251, 18
	v_readlane_b32 s75, v251, 19
	v_readlane_b32 s80, v251, 24
	v_readlane_b32 s81, v251, 25
	v_readlane_b32 s82, v251, 26
	v_readlane_b32 s83, v251, 27

.LBB0_436:
	s_andn2_b64 vcc, exec, s[50:51]
	s_cbranch_vccnz .LBB0_438
	s_ashr_i32 s4, s5, 31
	s_lshr_b32 s4, s4, 19
	s_add_i32 s4, s5, s4
	s_ashr_i32 s6, s4, 13
	s_and_b32 s4, s4, 0xe000
	s_sub_i32 s4, s33, s4
	s_add_i32 s7, s4, 0x880
	s_sext_i32_i16 s4, s7
	s_bfe_u32 s4, s4, 0x80017
	s_add_i32 s8, s7, s4
	s_sext_i32_i16 s4, s8
	s_and_b32 s8, s8, 0xff00
	s_sub_i32 s7, s7, s8
	s_sext_i32_i16 s11, s7
	s_ashr_i32 s7, s6, 31
	v_readlane_b32 s68, v251, 12
	s_ashr_i32 s4, s4, 8
	s_lshl_b64 s[8:9], s[6:7], 26
	v_readlane_b32 s70, v251, 14
	v_readlane_b32 s71, v251, 15
	s_add_u32 s42, s70, s8
	s_addc_u32 s43, s71, s9
	s_lshl_b64 s[6:7], s[6:7], 25
	v_readlane_b32 s8, v253, 30
	v_readlane_b32 s78, v251, 22
	v_readlane_b32 s79, v251, 23
	s_add_u32 s6, s8, s6
	v_readlane_b32 s8, v253, 31
	v_readlane_b32 s78, v250, 1
	s_addc_u32 s7, s8, s7
	s_lshl_b32 s48, s11, 5
	v_readlane_b32 s79, v250, 2
	s_movk_i32 s8, 0x800
	s_mov_b64 s[44:45], 0x2000
	s_mov_b32 s47, s48
	v_readlane_b32 s69, v251, 13
	v_readlane_b32 s72, v251, 16
	v_readlane_b32 s73, v251, 17
	v_readlane_b32 s74, v251, 18
	v_readlane_b32 s75, v251, 19
	v_readlane_b32 s76, v251, 20
	v_readlane_b32 s77, v251, 21
	v_readlane_b32 s80, v251, 24
	v_readlane_b32 s81, v251, 25
	v_readlane_b32 s82, v251, 26
	v_readlane_b32 s83, v251, 27

.LBB0_445:
	s_or_b64 exec, exec, s[8:9]
	s_mov_b32 s8, 0x3bfff
	v_cmp_lt_i32_e32 vcc, s8, v1
	v_add_u32_e32 v28, 0x110000, v28
	s_or_b64 s[6:7], vcc, s[6:7]
	v_add_u32_e32 v1, 0x44000, v1
	s_andn2_b64 exec, exec, s[6:7]
	s_cbranch_execz .LBB0_482

.LBB0_452:
	s_or_b64 exec, exec, s[8:9]
	v_add_u32_e32 v9, 0x11000, v1
	v_ashrrev_i32_e32 v11, 31, v9
	v_lshrrev_b32_e32 v10, 15, v11
	v_lshrrev_b32_e32 v11, 21, v11
	v_add_u32_e32 v11, v9, v11
	v_ashrrev_i32_e32 v11, 11, v11
	v_lshrrev_b32_e32 v12, 26, v11
	v_add_u32_e32 v12, v11, v12
	v_and_b32_e32 v12, 0xffffffc0, v12
	v_add_u32_e32 v10, v9, v10
	v_sub_u32_e32 v12, v11, v12
	v_mul_i32_i24_e32 v11, 0x800, v11
	s_mov_b32 s8, 0x6f000
	v_ashrrev_i32_e32 v10, 17, v10
	v_sub_u32_e32 v14, v9, v11
	v_cmp_gt_i32_e32 vcc, s8, v1
	v_mov_b32_e32 v9, 0
	v_mov_b32_e32 v13, 0
	s_and_saveexec_b64 s[8:9], vcc
	s_cbranch_execz .LBB0_460
	v_cmp_lt_i32_e32 vcc, 3, v12
	s_and_saveexec_b64 s[10:11], vcc
	s_xor_b64 s[10:11], exec, s[10:11]
	s_cbranch_execz .LBB0_457
	v_cmp_gt_u32_e32 vcc, 36, v12
	v_mov_b32_e32 v13, 0
	s_and_saveexec_b64 s[12:13], vcc
	s_cbranch_execz .LBB0_456
	v_ashrrev_i32_e32 v11, 31, v10
	v_readlane_b32 s48, v251, 31
	v_ashrrev_i32_e32 v15, 31, v14
	v_lshlrev_b64 v[16:17], 18, v[10:11]
	v_readlane_b32 s56, v251, 39
	v_readlane_b32 s57, v251, 40
	v_lshlrev_b64 v[18:19], 7, v[14:15]
	v_mov_b32_e32 v13, v3
	v_lshl_add_u64 v[16:17], s[56:57], 0, v[16:17]
	v_lshl_add_u64 v[16:17], v[16:17], 0, v[18:19]
	v_lshl_add_u64 v[16:17], v[12:13], 2, v[16:17]
	global_load_dword v13, v[16:17], off offset:-16
	v_readlane_b32 s49, v251, 32
	v_readlane_b32 s50, v251, 33
	v_readlane_b32 s51, v251, 34
	v_readlane_b32 s52, v251, 35
	v_readlane_b32 s53, v251, 36
	v_readlane_b32 s54, v251, 37
	v_readlane_b32 s55, v251, 38
	v_readlane_b32 s58, v251, 41
	v_readlane_b32 s59, v251, 42
	v_readlane_b32 s60, v251, 43
	v_readlane_b32 s61, v251, 44
	v_readlane_b32 s62, v251, 45
	v_readlane_b32 s63, v251, 46

.LBB0_460:
	s_or_b64 exec, exec, s[8:9]
	v_add_u32_e32 v11, 0x22000, v1
	v_ashrrev_i32_e32 v15, 31, v11
	v_lshrrev_b32_e32 v16, 15, v15
	v_lshrrev_b32_e32 v15, 21, v15
	v_add_u32_e32 v15, v11, v15
	v_ashrrev_i32_e32 v15, 11, v15
	v_lshrrev_b32_e32 v17, 26, v15
	v_add_u32_e32 v17, v15, v17
	v_and_b32_e32 v17, 0xffffffc0, v17
	v_add_u32_e32 v16, v11, v16
	v_sub_u32_e32 v18, v15, v17
	v_mul_i32_i24_e32 v15, 0x800, v15
	s_mov_b32 s8, 0x5e000
	v_ashrrev_i32_e32 v16, 17, v16
	v_sub_u32_e32 v20, v11, v15
	v_cmp_gt_i32_e32 vcc, s8, v1
	s_and_saveexec_b64 s[8:9], vcc
	s_cbranch_execz .LBB0_468
	v_cmp_lt_i32_e32 vcc, 3, v18
	s_and_saveexec_b64 s[10:11], vcc
	s_xor_b64 s[10:11], exec, s[10:11]
	s_cbranch_execz .LBB0_465
	v_cmp_gt_u32_e32 vcc, 36, v18
	v_mov_b32_e32 v9, 0
	s_and_saveexec_b64 s[12:13], vcc
	s_cbranch_execz .LBB0_464
	v_ashrrev_i32_e32 v17, 31, v16
	v_readlane_b32 s48, v251, 31
	v_ashrrev_i32_e32 v21, 31, v20
	v_lshlrev_b64 v[22:23], 18, v[16:17]
	v_readlane_b32 s56, v251, 39
	v_readlane_b32 s57, v251, 40
	v_lshlrev_b64 v[24:25], 7, v[20:21]
	v_mov_b32_e32 v19, v3
	v_lshl_add_u64 v[22:23], s[56:57], 0, v[22:23]
	v_lshl_add_u64 v[22:23], v[22:23], 0, v[24:25]
	v_lshl_add_u64 v[22:23], v[18:19], 2, v[22:23]
	global_load_dword v9, v[22:23], off offset:-16
	v_readlane_b32 s49, v251, 32
	v_readlane_b32 s50, v251, 33
	v_readlane_b32 s51, v251, 34
	v_readlane_b32 s52, v251, 35
	v_readlane_b32 s53, v251, 36
	v_readlane_b32 s54, v251, 37
	v_readlane_b32 s55, v251, 38
	v_readlane_b32 s58, v251, 41
	v_readlane_b32 s59, v251, 42
	v_readlane_b32 s60, v251, 43
	v_readlane_b32 s61, v251, 44
	v_readlane_b32 s62, v251, 45
	v_readlane_b32 s63, v251, 46

.LBB0_468:
	s_or_b64 exec, exec, s[8:9]
	v_add_u32_e32 v11, 0x33000, v1
	v_ashrrev_i32_e32 v15, 31, v11
	v_lshrrev_b32_e32 v17, 15, v15
	v_lshrrev_b32_e32 v15, 21, v15
	v_add_u32_e32 v15, v11, v15
	v_add_u32_e32 v17, v11, v17
	v_ashrrev_i32_e32 v15, 11, v15
	v_ashrrev_i32_e32 v22, 17, v17
	v_lshrrev_b32_e32 v17, 26, v15
	v_add_u32_e32 v17, v15, v17
	v_and_b32_e32 v17, 0xffffffc0, v17
	v_sub_u32_e32 v24, v15, v17
	v_mul_i32_i24_e32 v15, 0x800, v15
	s_mov_b32 s8, 0x4d000
	v_sub_u32_e32 v26, v11, v15
	v_cmp_gt_i32_e32 vcc, s8, v1
	v_mov_b32_e32 v15, 0
	s_and_saveexec_b64 s[8:9], vcc
	s_cbranch_execz .LBB0_476
	v_cmp_lt_i32_e32 vcc, 3, v24
	s_and_saveexec_b64 s[10:11], vcc
	s_xor_b64 s[10:11], exec, s[10:11]
	s_cbranch_execz .LBB0_473
	v_cmp_gt_u32_e32 vcc, 36, v24
	v_mov_b32_e32 v15, 0
	s_and_saveexec_b64 s[12:13], vcc
	s_cbranch_execz .LBB0_472
	v_ashrrev_i32_e32 v23, 31, v22
	v_readlane_b32 s48, v251, 31
	v_ashrrev_i32_e32 v27, 31, v26
	v_lshlrev_b64 v[30:31], 18, v[22:23]
	v_readlane_b32 s56, v251, 39
	v_readlane_b32 s57, v251, 40
	v_lshlrev_b64 v[32:33], 7, v[26:27]
	v_mov_b32_e32 v25, v3
	v_lshl_add_u64 v[30:31], s[56:57], 0, v[30:31]
	v_lshl_add_u64 v[30:31], v[30:31], 0, v[32:33]
	v_lshl_add_u64 v[30:31], v[24:25], 2, v[30:31]
	global_load_dword v15, v[30:31], off offset:-16
	v_readlane_b32 s49, v251, 32
	v_readlane_b32 s50, v251, 33
	v_readlane_b32 s51, v251, 34
	v_readlane_b32 s52, v251, 35
	v_readlane_b32 s53, v251, 36
	v_readlane_b32 s54, v251, 37
	v_readlane_b32 s55, v251, 38
	v_readlane_b32 s58, v251, 41
	v_readlane_b32 s59, v251, 42
	v_readlane_b32 s60, v251, 43
	v_readlane_b32 s61, v251, 44
	v_readlane_b32 s62, v251, 45
	v_readlane_b32 s63, v251, 46

.LBB0_476:
	s_or_b64 exec, exec, s[8:9]
	v_ashrrev_i32_e32 v30, 8, v8
	v_ashrrev_i32_e32 v31, 31, v30
	v_lshlrev_b64 v[4:5], 7, v[4:5]
	v_lshrrev_b32_e32 v17, 4, v8
	v_lshlrev_b32_e32 v2, 2, v2
	v_lshl_add_u64 v[4:5], v[30:31], 4, v[4:5]
	v_ashrrev_i32_e32 v32, 5, v6
	v_sub_u32_e32 v2, v28, v2
	v_and_or_b32 v4, v17, 15, v4
	v_readlane_b32 s8, v253, 38
	v_and_b32_e32 v2, 32, v2
	v_ashrrev_i32_e32 v33, 31, v32
	v_lshlrev_b64 v[4:5], 12, v[4:5]
	v_readlane_b32 s9, v253, 39
	v_and_or_b32 v2, v6, 31, v2
	v_lshlrev_b64 v[30:31], 11, v[32:33]
	v_lshl_add_u64 v[4:5], s[8:9], 0, v[4:5]
	s_waitcnt vmcnt(0)
	v_bfe_u32 v11, v7, 16, 1
	v_and_b32_e32 v8, 7, v8
	v_lshl_add_u64 v[4:5], v[4:5], 0, v[30:31]
	v_lshlrev_b32_e32 v2, 4, v2
	v_add3_u32 v11, v7, v11, s33
	v_lshl_add_u64 v[4:5], v[4:5], 0, v[2:3]
	v_lshlrev_b32_e32 v2, 1, v8
	v_lshl_add_u64 v[4:5], v[4:5], 0, v[2:3]
	v_and_b32_e32 v2, 0xffff0000, v11
	v_sub_f32_e32 v2, v7, v2
	v_bfe_u32 v6, v2, 16, 1
	s_mov_b32 s8, 0x6f000
	v_add3_u32 v2, v2, v6, s33
	v_cmp_gt_i32_e32 vcc, s8, v1
	global_store_short_d16_hi v[4:5], v11, off
	global_store_short_d16_hi v[4:5], v2, off offset:1024
	s_and_saveexec_b64 s[8:9], vcc
	s_cbranch_execz .LBB0_478
	v_lshlrev_b32_e32 v5, 2, v14
	v_ashrrev_i32_e32 v4, 8, v14
	v_and_b32_e32 v5, 32, v5
	v_ashrrev_i32_e32 v11, 31, v10
	v_bfe_u32 v2, v13, 16, 1
	v_ashrrev_i32_e32 v6, 5, v12
	v_and_or_b32 v12, v12, 31, v5
	v_ashrrev_i32_e32 v5, 31, v4
	v_lshlrev_b64 v[10:11], 7, v[10:11]
	v_add3_u32 v8, v13, v2, s33
	v_lshrrev_b32_e32 v2, 4, v14
	v_lshl_add_u64 v[4:5], v[4:5], 4, v[10:11]
	v_and_or_b32 v4, v2, 15, v4
	v_readlane_b32 s10, v253, 38
	v_ashrrev_i32_e32 v7, 31, v6
	v_lshlrev_b64 v[4:5], 12, v[4:5]
	v_readlane_b32 s11, v253, 39
	v_lshlrev_b64 v[6:7], 11, v[6:7]
	v_and_b32_e32 v17, 7, v14
	v_lshl_add_u64 v[4:5], s[10:11], 0, v[4:5]
	v_lshl_add_u64 v[4:5], v[4:5], 0, v[6:7]
	v_lshlrev_b32_e32 v2, 4, v12
	v_lshl_add_u64 v[4:5], v[4:5], 0, v[2:3]
	v_lshlrev_b32_e32 v2, 1, v17
	v_lshl_add_u64 v[4:5], v[4:5], 0, v[2:3]
	v_and_b32_e32 v2, 0xffff0000, v8
	v_sub_f32_e32 v2, v13, v2
	v_bfe_u32 v6, v2, 16, 1
	v_add3_u32 v2, v2, v6, s33
	global_store_short_d16_hi v[4:5], v8, off
	global_store_short_d16_hi v[4:5], v2, off offset:1024
.LBB0_478:
	s_or_b64 exec, exec, s[8:9]
	s_mov_b32 s8, 0x5e000
	v_cmp_gt_i32_e32 vcc, s8, v1
	s_and_saveexec_b64 s[8:9], vcc
	s_cbranch_execz .LBB0_480
	v_lshlrev_b32_e32 v5, 2, v20
	v_ashrrev_i32_e32 v4, 8, v20
	v_and_b32_e32 v5, 32, v5
	v_ashrrev_i32_e32 v17, 31, v16
	v_bfe_u32 v2, v9, 16, 1
	v_and_or_b32 v13, v18, 31, v5
	v_ashrrev_i32_e32 v5, 31, v4
	v_lshlrev_b64 v[10:11], 7, v[16:17]
	v_add3_u32 v8, v9, v2, s33
	v_lshrrev_b32_e32 v2, 4, v20
	v_lshl_add_u64 v[4:5], v[4:5], 4, v[10:11]
	v_ashrrev_i32_e32 v6, 5, v18
	v_and_or_b32 v4, v2, 15, v4
	v_readlane_b32 s10, v253, 38
	v_ashrrev_i32_e32 v7, 31, v6
	v_lshlrev_b64 v[4:5], 12, v[4:5]
	v_readlane_b32 s11, v253, 39
	v_lshlrev_b64 v[6:7], 11, v[6:7]
	v_and_b32_e32 v12, 7, v20
	v_lshl_add_u64 v[4:5], s[10:11], 0, v[4:5]
	v_lshl_add_u64 v[4:5], v[4:5], 0, v[6:7]
	v_lshlrev_b32_e32 v2, 4, v13
	v_lshl_add_u64 v[4:5], v[4:5], 0, v[2:3]
	v_lshlrev_b32_e32 v2, 1, v12
	v_lshl_add_u64 v[4:5], v[4:5], 0, v[2:3]
	v_and_b32_e32 v2, 0xffff0000, v8
	v_sub_f32_e32 v2, v9, v2
	v_bfe_u32 v6, v2, 16, 1
	v_add3_u32 v2, v2, v6, s33
	global_store_short_d16_hi v[4:5], v8, off
	global_store_short_d16_hi v[4:5], v2, off offset:1024
.LBB0_480:
	s_or_b64 exec, exec, s[8:9]
	s_mov_b32 s8, 0x4d000
	v_cmp_gt_i32_e32 vcc, s8, v1
	s_and_saveexec_b64 s[8:9], vcc
	s_cbranch_execz .LBB0_445
	v_lshlrev_b32_e32 v5, 2, v26
	v_ashrrev_i32_e32 v4, 8, v26
	v_and_b32_e32 v5, 32, v5
	v_ashrrev_i32_e32 v23, 31, v22
	v_bfe_u32 v2, v15, 16, 1
	v_and_or_b32 v12, v24, 31, v5
	v_ashrrev_i32_e32 v5, 31, v4
	v_lshlrev_b64 v[8:9], 7, v[22:23]
	v_add3_u32 v10, v15, v2, s33
	v_lshrrev_b32_e32 v2, 4, v26
	v_lshl_add_u64 v[4:5], v[4:5], 4, v[8:9]
	v_ashrrev_i32_e32 v6, 5, v24
	v_and_or_b32 v4, v2, 15, v4
	v_readlane_b32 s10, v253, 38
	v_ashrrev_i32_e32 v7, 31, v6
	v_lshlrev_b64 v[4:5], 12, v[4:5]
	v_readlane_b32 s11, v253, 39
	v_lshlrev_b64 v[6:7], 11, v[6:7]
	v_and_b32_e32 v11, 7, v26
	v_lshl_add_u64 v[4:5], s[10:11], 0, v[4:5]
	v_lshl_add_u64 v[4:5], v[4:5], 0, v[6:7]
	v_lshlrev_b32_e32 v2, 4, v12
	v_lshl_add_u64 v[4:5], v[4:5], 0, v[2:3]
	v_lshlrev_b32_e32 v2, 1, v11
	v_lshl_add_u64 v[4:5], v[4:5], 0, v[2:3]
	v_and_b32_e32 v2, 0xffff0000, v10
	v_sub_f32_e32 v2, v15, v2
	v_bfe_u32 v6, v2, 16, 1
	v_add3_u32 v2, v2, v6, s33
	global_store_short_d16_hi v[4:5], v10, off
	global_store_short_d16_hi v[4:5], v2, off offset:1024
	s_branch .LBB0_445
